# v55 + one static s_setprio 1 for waves 4-7 during the attention phase (P4), reset at its end
# baseline (speedup 1.0000x reference)
.LBB0_616:
	s_or_b64 exec, exec, s[2:3]
	v_readlane_b32 s2, v254, 63
	v_readlane_b32 s3, v255, 0
	s_and_b64 vcc, exec, s[2:3]
	s_barrier
	s_cbranch_vccnz .LBB0_712
	s_load_dwordx4 s[16:19], s[0:1], 0x110
	s_load_dwordx8 s[24:31], s[0:1], 0xf0
	s_load_dwordx4 s[36:39], s[0:1], 0x90
	s_mov_b32 s20, 0xfffe0000
	v_mbcnt_hi_u32_b32 v183, -1, v1
	s_mov_b32 s3, 0
	s_add_i32 s33, 0, 0x14800
	v_mov_b32_e32 v3, 0
	s_mov_b32 s52, 0xf800000
	v_mov_b32_e32 v182, 0x260
	s_mov_b64 s[4:5], 0x20000
	s_mov_b64 s[6:7], 0x40000
	s_mov_b64 s[8:9], 0x60000
	s_mov_b32 s21, -1
	s_mov_b32 s53, 0x41000000
	v_add_u32_e32 v184, -1, v183
	v_and_b32_e32 v185, 64, v183
	v_add_u32_e32 v186, -2, v183
	v_add_u32_e32 v187, -4, v183
	v_add_u32_e32 v188, -8, v183
	v_add_u32_e32 v189, -16, v183
	v_subrev_u32_e32 v190, 32, v183
	v_mov_b32_e32 v191, 0xff800000
	v_readlane_b32 s54, v254, 0
	v_readfirstlane_b32 s98, v0
	s_lshr_b32 s98, s98, 8
	s_cmp_lg_u32 s98, 0
	s_cbranch_scc0 .Lmy_prio_skip
	s_setprio 1
.Lmy_prio_skip:
	s_branch .LBB0_619
.LBB0_618:
	s_load_dword s2, s[0:1], 0x150
	s_waitcnt lgkmcnt(0)
	s_add_i32 s54, s54, s2
	s_cmpk_gt_i32 s54, 0xff
	s_cbranch_scc1 .LBB0_712

.LBB0_712:
	s_setprio 0
	s_getreg_b32 s6, hwreg(HW_REG_XCC_ID, 0, 4)
	s_waitcnt vmcnt(0)
	s_barrier
	s_mov_b64 s[2:3], exec
	v_readlane_b32 s4, v254, 1
	v_readlane_b32 s5, v254, 2
	s_and_b64 s[4:5], s[2:3], s[4:5]
	s_mov_b64 exec, s[4:5]
	s_cbranch_execz .LBB0_736
	s_add_i32 s7, 0, 0x22ff0
	v_mov_b32_e32 v2, s7
	s_load_dwordx2 s[4:5], s[0:1], 0x80
	s_waitcnt vmcnt(0) expcnt(0) lgkmcnt(0)
	ds_read_b32 v3, v2
	s_add_i32 s7, 0, 0x22ff4
	v_mov_b32_e32 v2, s7
	ds_read_b32 v2, v2
	s_and_b32 s20, s6, 15
	s_waitcnt lgkmcnt(1)
	v_cmp_ne_u32_e32 vcc, 0, v3
	s_cbranch_vccnz .LBB0_728
	v_readlane_b32 s6, v254, 3
	v_readlane_b32 s7, v254, 4
	s_load_dwordx2 s[10:11], s[6:7], 0x4
	s_load_dword s12, s[0:1], 0x150
	s_add_u32 s6, s4, 0x1000
	s_addc_u32 s7, s5, 0
	s_add_u32 s8, s4, 0x1100
	s_addc_u32 s9, s5, 0
	s_waitcnt lgkmcnt(0)
	s_mul_i32 s21, s10, s12
	s_add_u32 s10, s4, 0x1200
	s_mul_i32 s21, s21, s11
	s_addc_u32 s11, s5, 0
	s_add_u32 s12, s4, 0x1300
	s_addc_u32 s13, s5, 0
	s_mov_b32 s22, 1
	v_mov_b32_e32 v18, 0
	s_branch .LBB0_716
